# speedup vs baseline: 1.0086x; 1.0056x over previous
.LBB2_22:
	ds_read_b128 v[170:173], v174
	ds_read_b128 v[180:183], v174 offset:2048
	ds_read_b128 v[202:205], v178
	ds_read_b128 v[206:209], v178 offset:2048
	s_mov_b32 s89, s65
	s_mov_b32 s65, s6
	ds_read_b128 v[162:165], v194
	ds_read_b128 v[150:153], v194 offset:2048
	ds_read_b128 v[166:169], v195
	ds_read_b128 v[154:157], v195 offset:2048
	ds_read_b128 v[146:149], v194 offset:4096
	ds_read_b128 v[138:141], v194 offset:6144
	ds_read_b128 v[158:161], v195 offset:4096
	ds_read_b128 v[142:145], v195 offset:6144
	s_waitcnt vmcnt(14)
	s_mul_i32 s94, s83, s35
	v_cvt_pk_f16_f32 v22, v22, v23
	v_cvt_pk_f16_f32 v23, v24, v25
	v_cvt_pk_f16_f32 v18, v18, v19
	v_cvt_pk_f16_f32 v19, v20, v21
	s_lshl_b32 s6, s90, 6
	s_add_i32 s7, s94, s6
	s_lshl_b32 s7, s7, 2
	s_add_i32 s8, s7, s81
	ds_write2st64_b64 v201, v[22:23], v[18:19] offset0:32 offset1:40
	s_add_i32 s9, s8, s81
	s_add_i32 s10, s9, s81
	buffer_load_dwordx4 v[22:25], v192, s[56:59], s7 offen nt
	buffer_load_dwordx4 v[18:21], v192, s[56:59], s8 offen nt
	v_cvt_pk_f16_f32 v14, v14, v15
	v_cvt_pk_f16_f32 v15, v16, v17
	v_cvt_pk_f16_f32 v10, v10, v11
	v_cvt_pk_f16_f32 v11, v12, v13
	ds_write2st64_b64 v201, v[14:15], v[10:11] offset0:48 offset1:56
	buffer_load_dwordx4 v[14:17], v192, s[56:59], s9 offen nt
	buffer_load_dwordx4 v[10:13], v192, s[56:59], s10 offen nt
	s_nop 0
	s_waitcnt vmcnt(16)
	v_add_u32_e32 v210, s89, v193
	s_mul_i32 s95, s84, s35
	ds_write_b128 v210, v[6:9] offset:32768
	ds_write_b128 v210, v[2:5] offset:40960
	s_add_i32 s93, s95, s6
	s_nop 0
	s_barrier
	s_waitcnt lgkmcnt(0)
	s_setprio 1
	s_waitcnt lgkmcnt(11)
	v_mfma_f32_16x16x32_f16 v[134:137], v[170:173], v[162:165], v[134:137]
	v_mfma_f32_16x16x32_f16 v[130:133], v[180:183], v[162:165], v[130:133]
	s_waitcnt lgkmcnt(10)
	v_mfma_f32_16x16x32_f16 v[126:129], v[170:173], v[150:153], v[126:129]
	v_mfma_f32_16x16x32_f16 v[122:125], v[180:183], v[150:153], v[122:125]
	s_waitcnt lgkmcnt(7)
	v_mfma_f32_16x16x32_f16 v[118:121], v[170:173], v[146:149], v[118:121]
	v_mfma_f32_16x16x32_f16 v[114:117], v[180:183], v[146:149], v[114:117]
	s_waitcnt lgkmcnt(6)
	v_mfma_f32_16x16x32_f16 v[110:113], v[170:173], v[138:141], v[110:113]
	v_mfma_f32_16x16x32_f16 v[106:109], v[180:183], v[138:141], v[106:109]
	v_mfma_f32_16x16x32_f16 v[134:137], v[202:205], v[166:169], v[134:137]
	v_mfma_f32_16x16x32_f16 v[130:133], v[206:209], v[166:169], v[130:133]
	v_mfma_f32_16x16x32_f16 v[126:129], v[202:205], v[154:157], v[126:129]
	v_mfma_f32_16x16x32_f16 v[122:125], v[206:209], v[154:157], v[122:125]
	s_waitcnt lgkmcnt(5)
	v_mfma_f32_16x16x32_f16 v[118:121], v[202:205], v[158:161], v[118:121]
	v_mfma_f32_16x16x32_f16 v[114:117], v[206:209], v[158:161], v[114:117]
	s_waitcnt lgkmcnt(4)
	v_mfma_f32_16x16x32_f16 v[110:113], v[202:205], v[142:145], v[110:113]
	v_mfma_f32_16x16x32_f16 v[106:109], v[206:209], v[142:145], v[106:109]
	s_setprio 0
	s_barrier
	ds_read_b128 v[170:173], v174 offset:16384
	ds_read_b128 v[174:177], v174 offset:18432
	ds_read_b128 v[182:185], v178 offset:16384
	ds_read_b128 v[178:181], v178 offset:18432
	s_waitcnt vmcnt(14)
	s_cmp_lt_u32 s92, 32
	ds_write_b128 v210, v[30:33] offset:49152
	ds_write_b128 v210, v[26:29] offset:57344
	s_waitcnt vmcnt(13)
	s_cbranch_scc0 .LBB2_28
	s_add_i32 s38, s64, s92
	s_lshl_b64 s[60:61], s[38:39], 3
	s_add_u32 s60, s60, s85
	v_cmp_ne_u32_e64 s[6:7], 0, v34
	v_cmp_ne_u32_e64 s[8:9], 0, v35
	v_cmp_ne_u32_e64 s[10:11], 0, v36
	v_cmp_ne_u32_e64 s[12:13], 0, v37
	s_addc_u32 s61, s61, 0
	s_nop 1
	s_and_b64 s[98:99], s[6:7], s[8:9]
	s_and_b64 s[100:101], s[10:11], s[12:13]
	s_and_b64 s[98:99], s[98:99], s[100:101]
	s_cmp_eq_u64 s[98:99], -1
	s_cbranch_scc0 .Lqkv_mslow_0
	s_lshl_b64 s[96:97], s[60:61], 5
	v_lshl_add_u64 v[26:27], v[0:1], 0, s[96:97]
	v_mov_b32_e32 v28, -1
	v_mov_b32_e32 v29, -1
	s_add_u32 s6, s42, s60
	s_addc_u32 s7, s43, s61
	s_mov_b64 exec, 15
	global_store_dwordx2 v[26:27], v[28:29], off
	s_mov_b64 exec, 1
	global_store_byte v187, v187, s[6:7]
	s_mov_b64 exec, -1
	s_branch .LBB2_28
